# attention tile loops: wave-uniform branch test shortened (v_cndmask+v_cmp_ne ballot replaced by s_and_b64 vcc, mask, exec) at 3 sites
# baseline (speedup 1.0000x reference)
;     ...
;     const bool rb = fin && (mx > 8.f || st.fresh);
;     if (__any(rb)) { const float d = rb ? mx : 0.f; const float corr = st.fresh ? 1.f : __builtin_amdgcn_exp2f(-d); st.l *= corr; st.m += d;
; #pragma unroll
;         for (int i = 0; i < 16; ++i) { st.O[0][i] *= corr; st.O[1][i] *= corr; S0[i] -= d; S1[i] -= d; }
.LBB0_564:
	s_or_b64 exec, exec, s[30:31]
	s_and_b64 vcc, s[26:27], exec
	v_mov_b32_e32 v1, v224
	v_mov_b32_e32 v226, v225
	s_cbranch_vccz .LBB0_566
	v_cndmask_b32_e64 v14, 0, v14, s[26:27]
	v_exp_f32_e64 v1, -v14
	v_add_f32_e32 v226, v225, v14
	v_pk_add_f32 v[96:97], v[96:97], v[14:15] op_sel_hi:[1,0] neg_lo:[0,1] neg_hi:[0,1]
	v_pk_add_f32 v[80:81], v[80:81], v[14:15] op_sel_hi:[1,0] neg_lo:[0,1] neg_hi:[0,1]
	v_cndmask_b32_e64 v64, v1, 1.0, s[28:29]
	v_mul_f32_e32 v1, v224, v64
	v_pk_add_f32 v[98:99], v[98:99], v[14:15] op_sel_hi:[1,0] neg_lo:[0,1] neg_hi:[0,1]
	v_pk_add_f32 v[82:83], v[82:83], v[14:15] op_sel_hi:[1,0] neg_lo:[0,1] neg_hi:[0,1]
	v_pk_add_f32 v[100:101], v[100:101], v[14:15] op_sel_hi:[1,0] neg_lo:[0,1] neg_hi:[0,1]
	v_pk_add_f32 v[84:85], v[84:85], v[14:15] op_sel_hi:[1,0] neg_lo:[0,1] neg_hi:[0,1]
	v_pk_add_f32 v[102:103], v[102:103], v[14:15] op_sel_hi:[1,0] neg_lo:[0,1] neg_hi:[0,1]
	v_pk_add_f32 v[86:87], v[86:87], v[14:15] op_sel_hi:[1,0] neg_lo:[0,1] neg_hi:[0,1]
	v_pk_add_f32 v[104:105], v[104:105], v[14:15] op_sel_hi:[1,0] neg_lo:[0,1] neg_hi:[0,1]
	v_pk_add_f32 v[88:89], v[88:89], v[14:15] op_sel_hi:[1,0] neg_lo:[0,1] neg_hi:[0,1]
	v_pk_add_f32 v[106:107], v[106:107], v[14:15] op_sel_hi:[1,0] neg_lo:[0,1] neg_hi:[0,1]
	v_pk_add_f32 v[90:91], v[90:91], v[14:15] op_sel_hi:[1,0] neg_lo:[0,1] neg_hi:[0,1]
	v_pk_add_f32 v[108:109], v[108:109], v[14:15] op_sel_hi:[1,0] neg_lo:[0,1] neg_hi:[0,1]
	v_pk_add_f32 v[92:93], v[92:93], v[14:15] op_sel_hi:[1,0] neg_lo:[0,1] neg_hi:[0,1]
	v_pk_mul_f32 v[30:31], v[30:31], v[64:65] op_sel_hi:[1,0]
	v_pk_mul_f32 v[28:29], v[28:29], v[64:65] op_sel_hi:[1,0]
	v_pk_mul_f32 v[26:27], v[26:27], v[64:65] op_sel_hi:[1,0]
	v_pk_mul_f32 v[24:25], v[24:25], v[64:65] op_sel_hi:[1,0]
	v_pk_mul_f32 v[22:23], v[22:23], v[64:65] op_sel_hi:[1,0]
	v_pk_mul_f32 v[20:21], v[20:21], v[64:65] op_sel_hi:[1,0]
	v_pk_mul_f32 v[18:19], v[18:19], v[64:65] op_sel_hi:[1,0]
	v_pk_mul_f32 v[16:17], v[16:17], v[64:65] op_sel_hi:[1,0]
	v_pk_mul_f32 v[46:47], v[46:47], v[64:65] op_sel_hi:[1,0]
	v_pk_mul_f32 v[44:45], v[44:45], v[64:65] op_sel_hi:[1,0]
	v_pk_mul_f32 v[42:43], v[42:43], v[64:65] op_sel_hi:[1,0]
	v_pk_mul_f32 v[40:41], v[40:41], v[64:65] op_sel_hi:[1,0]
	v_pk_mul_f32 v[38:39], v[38:39], v[64:65] op_sel_hi:[1,0]
	v_pk_mul_f32 v[36:37], v[36:37], v[64:65] op_sel_hi:[1,0]
	v_pk_mul_f32 v[34:35], v[34:35], v[64:65] op_sel_hi:[1,0]
	v_pk_mul_f32 v[32:33], v[32:33], v[64:65] op_sel_hi:[1,0]
	v_pk_add_f32 v[110:111], v[110:111], v[14:15] op_sel_hi:[1,0] neg_lo:[0,1] neg_hi:[0,1]
	v_pk_add_f32 v[94:95], v[94:95], v[14:15] op_sel_hi:[1,0] neg_lo:[0,1] neg_hi:[0,1]

;     ...
;     if (__any(rb)) { const float d = rb ? mx : 0.f; const float corr = st.fresh ? 1.f : __builtin_amdgcn_exp2f(-d); st.l *= corr; st.m += d;
; #pragma unroll
;         for (int i = 0; i < 16; ++i) { st.O[0][i] *= corr; st.O[1][i] *= corr; S0[i] -= d; S1[i] -= d; }
;         if (IMP) { if (h == 0 && corr != 1.f) { for (int j = 0; j < 64; ++j) irow[j] *= corr; } }
.LBB0_575:
	s_or_b64 exec, exec, s[26:27]
	s_and_b64 vcc, s[30:31], exec
	s_cbranch_vccz .LBB0_579
	v_cndmask_b32_e64 v56, 0, v14, s[30:31]
	v_exp_f32_e64 v14, -v56
	s_nop 0
	v_cndmask_b32_e64 v14, v14, 1.0, s[28:29]
	v_cmp_neq_f32_e32 vcc, 1.0, v14
	s_and_b64 s[0:1], s[20:21], vcc
	s_and_saveexec_b64 s[26:27], s[0:1]
	s_cbranch_execz .LBB0_578
	ds_read2_b32 v[58:59], v223 offset1:1
	s_waitcnt lgkmcnt(0)
	v_pk_mul_f32 v[58:59], v[14:15], v[58:59] op_sel_hi:[0,1]
	ds_write2_b32 v223, v58, v59 offset1:1
	ds_read2_b32 v[58:59], v223 offset0:2 offset1:3
	s_waitcnt lgkmcnt(0)
	v_pk_mul_f32 v[58:59], v[14:15], v[58:59] op_sel_hi:[0,1]
	ds_write2_b32 v223, v58, v59 offset0:2 offset1:3
	ds_read2_b32 v[58:59], v223 offset0:4 offset1:5
	s_waitcnt lgkmcnt(0)
	v_pk_mul_f32 v[58:59], v[14:15], v[58:59] op_sel_hi:[0,1]
	ds_write2_b32 v223, v58, v59 offset0:4 offset1:5
	ds_read2_b32 v[58:59], v223 offset0:6 offset1:7
	s_waitcnt lgkmcnt(0)
	v_pk_mul_f32 v[58:59], v[14:15], v[58:59] op_sel_hi:[0,1]
	ds_write2_b32 v223, v58, v59 offset0:6 offset1:7
	ds_read2_b32 v[58:59], v223 offset0:8 offset1:9
	s_waitcnt lgkmcnt(0)
	v_pk_mul_f32 v[58:59], v[14:15], v[58:59] op_sel_hi:[0,1]
	ds_write2_b32 v223, v58, v59 offset0:8 offset1:9
	ds_read2_b32 v[58:59], v223 offset0:10 offset1:11
	s_waitcnt lgkmcnt(0)
	v_pk_mul_f32 v[58:59], v[14:15], v[58:59] op_sel_hi:[0,1]
	ds_write2_b32 v223, v58, v59 offset0:10 offset1:11
	ds_read2_b32 v[58:59], v223 offset0:12 offset1:13
	s_waitcnt lgkmcnt(0)
	v_pk_mul_f32 v[58:59], v[14:15], v[58:59] op_sel_hi:[0,1]
	ds_write2_b32 v223, v58, v59 offset0:12 offset1:13
	ds_read2_b32 v[58:59], v223 offset0:14 offset1:15
	s_waitcnt lgkmcnt(0)
	v_pk_mul_f32 v[58:59], v[14:15], v[58:59] op_sel_hi:[0,1]
	ds_write2_b32 v223, v58, v59 offset0:14 offset1:15
	ds_read2_b32 v[58:59], v223 offset0:16 offset1:17
	s_waitcnt lgkmcnt(0)
	v_pk_mul_f32 v[58:59], v[14:15], v[58:59] op_sel_hi:[0,1]
	ds_write2_b32 v223, v58, v59 offset0:16 offset1:17
	ds_read2_b32 v[58:59], v223 offset0:18 offset1:19
	s_waitcnt lgkmcnt(0)
	v_pk_mul_f32 v[58:59], v[14:15], v[58:59] op_sel_hi:[0,1]
	ds_write2_b32 v223, v58, v59 offset0:18 offset1:19
	ds_read2_b32 v[58:59], v223 offset0:20 offset1:21
	s_waitcnt lgkmcnt(0)
	v_pk_mul_f32 v[58:59], v[14:15], v[58:59] op_sel_hi:[0,1]
	ds_write2_b32 v223, v58, v59 offset0:20 offset1:21
	ds_read2_b32 v[58:59], v223 offset0:22 offset1:23
	s_waitcnt lgkmcnt(0)
	v_pk_mul_f32 v[58:59], v[14:15], v[58:59] op_sel_hi:[0,1]
	ds_write2_b32 v223, v58, v59 offset0:22 offset1:23
	ds_read2_b32 v[58:59], v223 offset0:24 offset1:25
	s_waitcnt lgkmcnt(0)
	v_pk_mul_f32 v[58:59], v[14:15], v[58:59] op_sel_hi:[0,1]
	ds_write2_b32 v223, v58, v59 offset0:24 offset1:25
	ds_read2_b32 v[58:59], v223 offset0:26 offset1:27
	s_waitcnt lgkmcnt(0)
	v_pk_mul_f32 v[58:59], v[14:15], v[58:59] op_sel_hi:[0,1]
	ds_write2_b32 v223, v58, v59 offset0:26 offset1:27
	ds_read2_b32 v[58:59], v223 offset0:28 offset1:29
	s_waitcnt lgkmcnt(0)
	v_pk_mul_f32 v[58:59], v[14:15], v[58:59] op_sel_hi:[0,1]
	ds_write2_b32 v223, v58, v59 offset0:28 offset1:29
	ds_read2_b32 v[58:59], v223 offset0:30 offset1:31
	s_waitcnt lgkmcnt(0)
	v_pk_mul_f32 v[58:59], v[14:15], v[58:59] op_sel_hi:[0,1]
	ds_write2_b32 v223, v58, v59 offset0:30 offset1:31
	ds_read2_b32 v[58:59], v223 offset0:32 offset1:33
	s_waitcnt lgkmcnt(0)
	v_pk_mul_f32 v[58:59], v[14:15], v[58:59] op_sel_hi:[0,1]
	ds_write2_b32 v223, v58, v59 offset0:32 offset1:33
	ds_read2_b32 v[58:59], v223 offset0:34 offset1:35
	s_waitcnt lgkmcnt(0)
	v_pk_mul_f32 v[58:59], v[14:15], v[58:59] op_sel_hi:[0,1]
	ds_write2_b32 v223, v58, v59 offset0:34 offset1:35
	ds_read2_b32 v[58:59], v223 offset0:36 offset1:37
	s_waitcnt lgkmcnt(0)
	v_pk_mul_f32 v[58:59], v[14:15], v[58:59] op_sel_hi:[0,1]
	ds_write2_b32 v223, v58, v59 offset0:36 offset1:37
	ds_read2_b32 v[58:59], v223 offset0:38 offset1:39
	s_waitcnt lgkmcnt(0)
	v_pk_mul_f32 v[58:59], v[14:15], v[58:59] op_sel_hi:[0,1]
	ds_write2_b32 v223, v58, v59 offset0:38 offset1:39
	ds_read2_b32 v[58:59], v223 offset0:40 offset1:41
	s_waitcnt lgkmcnt(0)
	v_pk_mul_f32 v[58:59], v[14:15], v[58:59] op_sel_hi:[0,1]
	ds_write2_b32 v223, v58, v59 offset0:40 offset1:41
	ds_read2_b32 v[58:59], v223 offset0:42 offset1:43
	s_waitcnt lgkmcnt(0)
	v_pk_mul_f32 v[58:59], v[14:15], v[58:59] op_sel_hi:[0,1]
	ds_write2_b32 v223, v58, v59 offset0:42 offset1:43
	ds_read2_b32 v[58:59], v223 offset0:44 offset1:45
	s_waitcnt lgkmcnt(0)
	v_pk_mul_f32 v[58:59], v[14:15], v[58:59] op_sel_hi:[0,1]
	ds_write2_b32 v223, v58, v59 offset0:44 offset1:45
	ds_read2_b32 v[58:59], v223 offset0:46 offset1:47
	s_waitcnt lgkmcnt(0)
	v_pk_mul_f32 v[58:59], v[14:15], v[58:59] op_sel_hi:[0,1]
	ds_write2_b32 v223, v58, v59 offset0:46 offset1:47
	ds_read2_b32 v[58:59], v223 offset0:48 offset1:49
	s_waitcnt lgkmcnt(0)
	v_pk_mul_f32 v[58:59], v[14:15], v[58:59] op_sel_hi:[0,1]
	ds_write2_b32 v223, v58, v59 offset0:48 offset1:49
	ds_read2_b32 v[58:59], v223 offset0:50 offset1:51
	s_waitcnt lgkmcnt(0)
	v_pk_mul_f32 v[58:59], v[14:15], v[58:59] op_sel_hi:[0,1]
	ds_write2_b32 v223, v58, v59 offset0:50 offset1:51
	ds_read2_b32 v[58:59], v223 offset0:52 offset1:53
	s_waitcnt lgkmcnt(0)
	v_pk_mul_f32 v[58:59], v[14:15], v[58:59] op_sel_hi:[0,1]
	ds_write2_b32 v223, v58, v59 offset0:52 offset1:53
	ds_read2_b32 v[58:59], v223 offset0:54 offset1:55
	s_waitcnt lgkmcnt(0)
	v_pk_mul_f32 v[58:59], v[14:15], v[58:59] op_sel_hi:[0,1]
	ds_write2_b32 v223, v58, v59 offset0:54 offset1:55
	ds_read2_b32 v[58:59], v223 offset0:56 offset1:57
	s_waitcnt lgkmcnt(0)
	v_pk_mul_f32 v[58:59], v[14:15], v[58:59] op_sel_hi:[0,1]
	ds_write2_b32 v223, v58, v59 offset0:56 offset1:57
	ds_read2_b32 v[58:59], v223 offset0:58 offset1:59
	s_waitcnt lgkmcnt(0)
	v_pk_mul_f32 v[58:59], v[14:15], v[58:59] op_sel_hi:[0,1]
	ds_write2_b32 v223, v58, v59 offset0:58 offset1:59
	ds_read2_b32 v[58:59], v223 offset0:60 offset1:61
	s_waitcnt lgkmcnt(0)
	v_pk_mul_f32 v[58:59], v[14:15], v[58:59] op_sel_hi:[0,1]
	ds_write2_b32 v223, v58, v59 offset0:60 offset1:61
	ds_read2_b32 v[58:59], v223 offset0:62 offset1:63
	s_waitcnt lgkmcnt(0)
	v_pk_mul_f32 v[58:59], v[14:15], v[58:59] op_sel_hi:[0,1]
	ds_write2_b32 v223, v58, v59 offset0:62 offset1:63

;     ...
;     const bool rb = fin && (mx > 8.f || st.fresh);
;     if (__any(rb)) { const float d = rb ? mx : 0.f; const float corr = st.fresh ? 1.f : __builtin_amdgcn_exp2f(-d); st.l *= corr; st.m += d;
; #pragma unroll
;         for (int i = 0; i < 16; ++i) { st.O[0][i] *= corr; st.O[1][i] *= corr; S0[i] -= d; S1[i] -= d; }
.LBB0_618:
	s_or_b64 exec, exec, s[88:89]
	s_and_b64 vcc, s[76:77], exec
	s_cbranch_vccz .LBB0_620
	v_cndmask_b32_e64 v14, 0, v14, s[76:77]
	v_exp_f32_e64 v15, -v14
	v_add_f32_e32 v154, v154, v14
	v_cndmask_b32_e64 v156, v15, 1.0, s[90:91]
	v_pk_add_f32 v[64:65], v[64:65], v[14:15] op_sel_hi:[1,0] neg_lo:[0,1] neg_hi:[0,1]
	v_pk_add_f32 v[48:49], v[48:49], v[14:15] op_sel_hi:[1,0] neg_lo:[0,1] neg_hi:[0,1]
	v_mul_f32_e32 v1, v1, v156
	v_pk_add_f32 v[66:67], v[66:67], v[14:15] op_sel_hi:[1,0] neg_lo:[0,1] neg_hi:[0,1]
	v_pk_add_f32 v[50:51], v[50:51], v[14:15] op_sel_hi:[1,0] neg_lo:[0,1] neg_hi:[0,1]
	v_pk_add_f32 v[68:69], v[68:69], v[14:15] op_sel_hi:[1,0] neg_lo:[0,1] neg_hi:[0,1]
	v_pk_add_f32 v[52:53], v[52:53], v[14:15] op_sel_hi:[1,0] neg_lo:[0,1] neg_hi:[0,1]
	v_pk_add_f32 v[70:71], v[70:71], v[14:15] op_sel_hi:[1,0] neg_lo:[0,1] neg_hi:[0,1]
	v_pk_add_f32 v[54:55], v[54:55], v[14:15] op_sel_hi:[1,0] neg_lo:[0,1] neg_hi:[0,1]
	v_pk_add_f32 v[72:73], v[72:73], v[14:15] op_sel_hi:[1,0] neg_lo:[0,1] neg_hi:[0,1]
	v_pk_add_f32 v[56:57], v[56:57], v[14:15] op_sel_hi:[1,0] neg_lo:[0,1] neg_hi:[0,1]
	v_pk_add_f32 v[74:75], v[74:75], v[14:15] op_sel_hi:[1,0] neg_lo:[0,1] neg_hi:[0,1]
	v_pk_add_f32 v[58:59], v[58:59], v[14:15] op_sel_hi:[1,0] neg_lo:[0,1] neg_hi:[0,1]
	v_pk_add_f32 v[76:77], v[76:77], v[14:15] op_sel_hi:[1,0] neg_lo:[0,1] neg_hi:[0,1]
	v_pk_add_f32 v[60:61], v[60:61], v[14:15] op_sel_hi:[1,0] neg_lo:[0,1] neg_hi:[0,1]
	v_pk_mul_f32 v[30:31], v[30:31], v[156:157] op_sel_hi:[1,0]
	v_pk_mul_f32 v[28:29], v[28:29], v[156:157] op_sel_hi:[1,0]
	v_pk_mul_f32 v[26:27], v[26:27], v[156:157] op_sel_hi:[1,0]
	v_pk_mul_f32 v[24:25], v[24:25], v[156:157] op_sel_hi:[1,0]
	v_pk_mul_f32 v[22:23], v[22:23], v[156:157] op_sel_hi:[1,0]
	v_pk_mul_f32 v[20:21], v[20:21], v[156:157] op_sel_hi:[1,0]
	v_pk_mul_f32 v[18:19], v[18:19], v[156:157] op_sel_hi:[1,0]
	v_pk_mul_f32 v[16:17], v[16:17], v[156:157] op_sel_hi:[1,0]
	v_pk_mul_f32 v[46:47], v[46:47], v[156:157] op_sel_hi:[1,0]
	v_pk_mul_f32 v[44:45], v[44:45], v[156:157] op_sel_hi:[1,0]
	v_pk_mul_f32 v[42:43], v[42:43], v[156:157] op_sel_hi:[1,0]
	v_pk_mul_f32 v[40:41], v[40:41], v[156:157] op_sel_hi:[1,0]
	v_pk_mul_f32 v[38:39], v[38:39], v[156:157] op_sel_hi:[1,0]
	v_pk_mul_f32 v[36:37], v[36:37], v[156:157] op_sel_hi:[1,0]
	v_pk_mul_f32 v[34:35], v[34:35], v[156:157] op_sel_hi:[1,0]
	v_pk_mul_f32 v[32:33], v[32:33], v[156:157] op_sel_hi:[1,0]
	v_pk_add_f32 v[78:79], v[78:79], v[14:15] op_sel_hi:[1,0] neg_lo:[0,1] neg_hi:[0,1]
	v_pk_add_f32 v[62:63], v[62:63], v[14:15] op_sel_hi:[1,0] neg_lo:[0,1] neg_hi:[0,1]
